# baseline (speedup 1.0000x reference)
.Lp_top:
	s_setprio 3
	v_readfirstlane_b32 s34, v10
	s_cmp_lt_u32 s34, s62
	s_cselect_b32 s45, s64, s65
	s_cselect_b32 s46, 0, s62
	s_cselect_b32 s48, s62, s63
	s_sub_u32 s47, s34, s46
	s_cmp_ge_u32 s47, s48
	s_cbranch_scc1 .Lp_done
	s_lshl_b32 s47, s47, 3
	s_add_u32 s45, s45, s47
	v_mov_b32_e32 v11, s45
	ds_read2_b32 v[12:13], v11 offset1:1
	s_waitcnt lgkmcnt(0)
	v_readfirstlane_b32 s35, v12
	v_readfirstlane_b32 s36, v13
	s_nop 1
	v_mov_b32_e32 v10, s35
	v_mov_b32_e32 v11, s36
	v_cndmask_b32_e64 v12, v10, v11, s[54:55]
	v_cndmask_b32_e64 v13, v10, v11, s[56:57]
	v_lshl_add_u32 v12, v12, 3, v61
	v_lshl_add_u32 v14, v13, 4, v62
	ds_read_b64 v[2:3], v12
	ds_read_b128 v[4:7], v14
	v_mad_u32_u24 v9, v13, s49, v58
	v_mov_b32_e32 v8, v56
	s_waitcnt lgkmcnt(0)
	v_add_u32_e32 v2, v2, v55
	v_and_b32_e32 v3, v3, v63
	s_nop 0
	v_readlane_b32 s41, v3, 0
	v_readlane_b32 s42, v3, 4
	s_max_u32 s43, s41, s42
	s_cmp_eq_u32 s43, 0
	s_cbranch_scc1 .Lp_zero
	ds_read_b64 v[36:37], v2
	v_cmp_gt_u32_e32 vcc, v3, v8
	v_add_u32_e32 v2, 64, v2
	v_add_u32_e32 v8, 16, v8
	v_mov_b32_e32 v33, 0x3c00
	s_waitcnt lgkmcnt(0)
	v_perm_b32 v32, v37, v36, v57
	v_cndmask_b32_e32 v33, 0, v33, vcc
	s_nop 0
	v_cndmask_b32_e32 v32, 0, v32, vcc
	s_nop 1
	v_mfma_f32_32x32x16_f16 v[96:111], v[32:35], v[64:67], 0
	v_mfma_f32_32x32x16_f16 v[112:127], v[32:35], v[68:71], 0
	s_setprio 0
	s_nop 10
	s_mov_b32 s45, s43
	s_min_u32 s46, s45, 16
	s_cmp_eq_u32 s46, 16
	s_cbranch_scc1 .Lf16
	s_cmp_eq_u32 s46, 15
	s_cbranch_scc1 .Lf15
	s_cmp_eq_u32 s46, 14
	s_cbranch_scc1 .Lf14
	s_cmp_eq_u32 s46, 13
	s_cbranch_scc1 .Lf13
	s_cmp_eq_u32 s46, 12
	s_cbranch_scc1 .Lf12
	s_cmp_eq_u32 s46, 11
	s_cbranch_scc1 .Lf11
	s_cmp_eq_u32 s46, 10
	s_cbranch_scc1 .Lf10
	s_cmp_eq_u32 s46, 9
	s_cbranch_scc1 .Lf9
	s_cmp_eq_u32 s46, 8
	s_cbranch_scc1 .Lf8
	s_cmp_eq_u32 s46, 7
	s_cbranch_scc1 .Lf7
	s_cmp_eq_u32 s46, 6
	s_cbranch_scc1 .Lf6
	s_cmp_eq_u32 s46, 5
	s_cbranch_scc1 .Lf5
	s_cmp_eq_u32 s46, 4
	s_cbranch_scc1 .Lf4
	s_cmp_eq_u32 s46, 3
	s_cbranch_scc1 .Lf3
	s_cmp_eq_u32 s46, 2
	s_cbranch_scc1 .Lf2

.Lsub:
	s_setprio 3
	ds_read_b64 v[36:37], v2
	v_cmp_gt_u32_e32 vcc, v3, v8
	v_add_u32_e32 v2, 64, v2
	v_add_u32_e32 v8, 16, v8
	v_mov_b32_e32 v33, 0x3c00
	s_waitcnt lgkmcnt(0)
	v_perm_b32 v32, v37, v36, v57
	v_cndmask_b32_e32 v33, 0, v33, vcc
	s_nop 0
	v_cndmask_b32_e32 v32, 0, v32, vcc
	s_nop 1
	v_mfma_f32_32x32x16_f16 v[96:111], v[32:35], v[64:67], 0
	v_mfma_f32_32x32x16_f16 v[112:127], v[32:35], v[68:71], 0
	s_setprio 2
	s_nop 10
	s_sub_u32 s45, s43, s44
	s_min_u32 s46, s45, 16
	s_cmp_eq_u32 s46, 2
	s_cbranch_scc1 .Ln2
	s_cmp_eq_u32 s46, 3
	s_cbranch_scc1 .Ln3
	s_cmp_eq_u32 s46, 4
	s_cbranch_scc1 .Ln4
	s_cmp_eq_u32 s46, 5
	s_cbranch_scc1 .Ln5
	s_cmp_eq_u32 s46, 6
	s_cbranch_scc1 .Ln6
	s_cmp_eq_u32 s46, 7
	s_cbranch_scc1 .Ln7
	s_cmp_eq_u32 s46, 8
	s_cbranch_scc1 .Ln8
	s_cmp_eq_u32 s46, 9
	s_cbranch_scc1 .Ln9
	s_cmp_eq_u32 s46, 10
	s_cbranch_scc1 .Ln10
	s_cmp_eq_u32 s46, 11
	s_cbranch_scc1 .Ln11
	s_cmp_eq_u32 s46, 12
	s_cbranch_scc1 .Ln12
	s_cmp_eq_u32 s46, 13
	s_cbranch_scc1 .Ln13
	s_cmp_eq_u32 s46, 14
	s_cbranch_scc1 .Ln14
	s_cmp_eq_u32 s46, 15
	s_cbranch_scc1 .Ln15
	s_cmp_eq_u32 s46, 16
	s_cbranch_scc1 .Ln16
